# plus attention exp scale folded into the logit scale (64 fewer v_mul per item) and 4x unrolled x to bf16 conversion
# speedup vs baseline: 1.0105x; 1.0105x over previous
.LBB0_75:
	s_or_b64 exec, exec, s[12:13]
	s_mov_b32 s4, 0x400000
	v_cmp_gt_i32_e32 vcc, s4, v0
	v_ashrrev_i32_e32 v1, 31, v0
	s_and_saveexec_b64 s[4:5], vcc
	s_cbranch_execz .LBB0_78
	s_load_dwordx2 s[10:11], s[8:9], 0x0
	v_lshl_add_u64 v[2:3], v[0:1], 4, s[6:7]
	s_mov_b64 s[12:13], 0x1f600000
	s_ashr_i32 s15, s14, 31
	v_lshl_add_u64 v[2:3], v[2:3], 0, s[12:13]
	s_lshl_b64 s[12:13], s[14:15], 4
	v_lshlrev_b32_e32 v4, 1, v0
	s_lshl_b32 s3, s3, 10
	s_mov_b64 s[16:17], 0
	s_mov_b32 s15, 0x3fffff
	v_mov_b32_e32 v6, v0
	s_waitcnt lgkmcnt(0)
	s_mul_i32 s18, s14, 3
	s_mov_b64 s[22:23], exec
	s_lshl_b32 s24, s3, 4
	s_mov_b32 s25, 0
.Lx4_loop:
	v_add_u32_e32 v176, s18, v6
	v_cmp_ge_i32_e32 vcc, s15, v176
	s_and_b64 exec, exec, vcc
	s_cbranch_execz .Lx4_done
	v_ashrrev_i32_e32 v5, 31, v4
	v_lshl_add_u64 v[178:179], v[4:5], 4, s[10:11]
	v_lshl_add_u64 v[180:181], v[178:179], 0, s[24:25]
	v_lshl_add_u64 v[182:183], v[180:181], 0, s[24:25]
	v_lshl_add_u64 v[184:185], v[182:183], 0, s[24:25]
	global_load_dwordx4 v[188:191], v[178:179], off
	global_load_dwordx4 v[192:195], v[178:179], off offset:16
	global_load_dwordx4 v[196:199], v[180:181], off
	global_load_dwordx4 v[200:203], v[180:181], off offset:16
	global_load_dwordx4 v[204:207], v[182:183], off
	global_load_dwordx4 v[208:211], v[182:183], off offset:16
	global_load_dwordx4 v[212:215], v[184:185], off
	global_load_dwordx4 v[216:219], v[184:185], off offset:16
	v_lshl_add_u32 v6, s14, 2, v6
	v_lshl_add_u32 v4, s3, 2, v4
	s_waitcnt vmcnt(6)
	v_cvt_pk_bf16_f32 v188, v188, v189
	v_cvt_pk_bf16_f32 v189, v190, v191
	v_cvt_pk_bf16_f32 v190, v192, v193
	v_cvt_pk_bf16_f32 v191, v194, v195
	global_store_dwordx4 v[2:3], v[188:191], off
	v_lshl_add_u64 v[2:3], v[2:3], 0, s[12:13]
	s_waitcnt vmcnt(5)
	v_cvt_pk_bf16_f32 v196, v196, v197
	v_cvt_pk_bf16_f32 v197, v198, v199
	v_cvt_pk_bf16_f32 v198, v200, v201
	v_cvt_pk_bf16_f32 v199, v202, v203
	global_store_dwordx4 v[2:3], v[196:199], off
	v_lshl_add_u64 v[2:3], v[2:3], 0, s[12:13]
	s_waitcnt vmcnt(4)
	v_cvt_pk_bf16_f32 v204, v204, v205
	v_cvt_pk_bf16_f32 v205, v206, v207
	v_cvt_pk_bf16_f32 v206, v208, v209
	v_cvt_pk_bf16_f32 v207, v210, v211
	global_store_dwordx4 v[2:3], v[204:207], off
	v_lshl_add_u64 v[2:3], v[2:3], 0, s[12:13]
	s_waitcnt vmcnt(3)
	v_cvt_pk_bf16_f32 v212, v212, v213
	v_cvt_pk_bf16_f32 v213, v214, v215
	v_cvt_pk_bf16_f32 v214, v216, v217
	v_cvt_pk_bf16_f32 v215, v218, v219
	global_store_dwordx4 v[2:3], v[212:215], off
	v_lshl_add_u64 v[2:3], v[2:3], 0, s[12:13]
	s_branch .Lx4_loop
.Lx4_done:
	s_mov_b64 exec, s[22:23]
	v_cmp_ge_i32_e32 vcc, s15, v6
	s_and_b64 exec, exec, vcc
	s_cbranch_execz .LBB0_78

.LBB0_142:
	s_add_u32 s0, s90, 0xc8
	s_addc_u32 s1, s91, 0
	v_writelane_b32 v253, s0, 3
	s_ashr_i32 s80, s2, 31
	v_mbcnt_lo_u32_b32 v0, -1, 0
	v_writelane_b32 v253, s1, 4
	s_lshr_b32 s0, s80, 29
	s_add_i32 s0, s2, s0
	s_ashr_i32 s6, s0, 3
	s_and_b32 s0, s0, -8
	s_sub_i32 s1, s2, s0
	v_readlane_b32 s0, v253, 0
	s_cmp_eq_u32 s0, 0
	s_cselect_b64 s[4:5], -1, 0
	v_writelane_b32 v253, s4, 5
	s_cmp_eq_u32 s67, 15
	s_movk_i32 s79, 0x200
	v_writelane_b32 v253, s5, 6
	s_cselect_b64 s[4:5], -1, 0
	v_writelane_b32 v253, s4, 7
	s_cmp_eq_u32 s67, 14
	s_mov_b32 s73, 0x200000
	v_writelane_b32 v253, s5, 8
	s_cselect_b64 s[4:5], -1, 0
	v_writelane_b32 v253, s4, 9
	s_cmp_eq_u32 s67, 13
	s_movk_i32 s97, 0x400
	v_writelane_b32 v253, s5, 10
	s_cselect_b64 s[4:5], -1, 0
	v_writelane_b32 v253, s4, 11
	s_cmp_eq_u32 s67, 12
	v_mov_b32_e32 v137, 0
	v_writelane_b32 v253, s5, 12
	s_cselect_b64 s[4:5], -1, 0
	v_writelane_b32 v253, s4, 13
	s_cmp_eq_u32 s67, 11
	s_movk_i32 s74, 0x4000
	v_writelane_b32 v253, s5, 14
	s_cselect_b64 s[4:5], -1, 0
	v_writelane_b32 v253, s4, 15
	s_cmp_eq_u32 s67, 10
	s_movk_i32 s82, 0x6000
	v_writelane_b32 v253, s5, 16
	s_cselect_b64 s[4:5], -1, 0
	v_writelane_b32 v253, s4, 17
	s_cmp_eq_u32 s67, 9
	v_mov_b32_e32 v186, 0x1000
	v_writelane_b32 v253, s5, 18
	s_cselect_b64 s[4:5], -1, 0
	v_writelane_b32 v253, s4, 19
	s_cmp_eq_u32 s67, 8
	v_mov_b32_e32 v187, 1
	v_writelane_b32 v253, s5, 20
	s_cselect_b64 s[4:5], -1, 0
	v_writelane_b32 v253, s4, 21
	s_cmp_eq_u32 s67, 7
	v_mov_b32_e32 v252, 0x2000
	v_writelane_b32 v253, s5, 22
	s_cselect_b64 s[4:5], -1, 0
	v_writelane_b32 v253, s4, 23
	s_cmp_eq_u32 s67, 6
	v_mov_b32_e32 v194, 0x3000
	v_writelane_b32 v253, s5, 24
	s_cselect_b64 s[4:5], -1, 0
	v_writelane_b32 v253, s4, 25
	s_cmp_eq_u32 s67, 5
	v_mov_b32_e32 v190, 0x23e00000
	v_writelane_b32 v253, s5, 26
	s_cselect_b64 s[4:5], -1, 0
	v_writelane_b32 v253, s4, 27
	s_cmp_eq_u32 s67, 4
	s_movk_i32 s75, 0x1ff
	v_writelane_b32 v253, s5, 28
	s_cselect_b64 s[4:5], -1, 0
	v_writelane_b32 v253, s4, 29
	s_cmp_eq_u32 s67, 3
	s_movk_i32 s35, 0x100
	v_writelane_b32 v253, s5, 30
	s_cselect_b64 s[4:5], -1, 0
	v_writelane_b32 v253, s4, 31
	s_cmp_eq_u32 s67, 2
	s_movk_i32 s62, 0x120
	v_writelane_b32 v253, s5, 32
	s_cselect_b64 s[4:5], -1, 0
	v_writelane_b32 v253, s4, 33
	s_cmp_eq_u32 s67, 1
	s_mov_b32 s17, 0xf149f2ca
	v_writelane_b32 v253, s5, 34
	s_cselect_b64 s[4:5], -1, 0
	v_writelane_b32 v253, s4, 35
	s_cmp_eq_u32 s67, 0
	v_mov_b32_e32 v191, 0x260
	v_writelane_b32 v253, s5, 36
	s_cselect_b64 s[4:5], -1, 0
	v_writelane_b32 v253, s4, 37
	s_lshl_b32 s0, s67, 6
	v_mov_b32_e32 v192, 0x3727c5ac
	v_writelane_b32 v253, s5, 38
	v_writelane_b32 v253, s0, 39
	s_lshl_b32 s0, s2, 3
	v_writelane_b32 v253, s0, 40
	s_not_b32 s0, s2
	s_cmpk_lt_i32 s2, 0x800
	v_writelane_b32 v253, s0, 41
	s_cselect_b64 s[4:5], -1, 0
	v_writelane_b32 v253, s4, 42
	s_lshl_b32 s0, s2, 9
	s_cmpk_lt_i32 s2, 0x200
	v_writelane_b32 v253, s5, 43
	v_writelane_b32 v253, s0, 44
	s_cselect_b64 s[4:5], -1, 0
	v_writelane_b32 v253, s4, 45
	s_lshr_b32 s3, s1, 31
	s_lshl_b32 s0, s1, 6
	v_writelane_b32 v253, s5, 46
	v_writelane_b32 v253, s3, 47
	s_cmp_lt_i32 s1, 0
	v_writelane_b32 v253, s1, 48
	s_mulk_i32 s1, 0x41
	s_cselect_b32 s0, s1, s0
	s_add_i32 s0, s0, s6
	s_ashr_i32 s1, s0, 31
	s_lshr_b32 s1, s1, 26
	s_add_i32 s1, s0, s1
	s_ashr_i32 s3, s1, 6
	s_and_b32 s1, s1, 0xffc0
	s_sub_i32 s1, s0, s1
	s_bfe_i32 s0, s1, 0x80000
	s_bfe_u32 s0, s0, 0x3000c
	s_lshl_b32 s5, s3, 3
	s_add_i32 s3, s1, s0
	s_bfe_i32 s0, s3, 0x80000
	s_and_b32 s3, s3, 0xf8
	s_sub_i32 s1, s1, s3
	s_sext_i32_i16 s4, s0
	s_sext_i32_i8 s1, s1
	s_lshr_b32 s0, s4, 3
	s_add_i32 s8, s5, s1
	s_ashr_i32 s1, s4, 3
	v_writelane_b32 v253, s1, 49
	s_bfe_i64 s[0:1], s[0:1], 0x100000
	s_lshl_b64 s[0:1], s[0:1], 20
	v_writelane_b32 v253, s0, 50
	s_ashr_i32 s9, s8, 31
	s_lshl_b64 s[4:5], s[8:9], 20
	v_writelane_b32 v253, s1, 51
	s_lshr_b32 s0, s80, 30
	s_add_i32 s0, s2, s0
	s_ashr_i32 s0, s0, 2
	v_writelane_b32 v253, s0, 52
	s_lshl_b32 s0, s0, 8
	v_writelane_b32 v253, s0, 53
	s_add_i32 s0, 0, 0x27fc0
	v_writelane_b32 v253, s0, 54
	s_add_i32 s0, 0, 0x27fc4
	v_writelane_b32 v253, s0, 55
	s_add_i32 s0, 0, 0x20000
	v_writelane_b32 v253, s0, 56
	s_add_i32 s0, 0, 0x21000
	v_writelane_b32 v253, s0, 57
	s_add_i32 s0, 0, 0xd100
	v_writelane_b32 v253, s0, 58
	s_add_i32 s0, 0, 0x13400
	v_writelane_b32 v253, s0, 59
	s_add_i32 s0, 0, 0x13500
	v_writelane_b32 v253, s0, 60
	s_add_i32 s0, 0, 0x13600
	v_writelane_b32 v253, s0, 61
	s_add_i32 s0, 0, 0x13700
	v_writelane_b32 v253, s0, 62
	s_add_i32 s0, 0, 0x14200
	v_writelane_b32 v253, s0, 63
	s_add_i32 s0, 0, 0x13800
	v_writelane_b32 v254, s0, 0
	s_add_i32 s0, 0, 0x13900
	v_writelane_b32 v254, s0, 1
	s_add_i32 s0, 0, 0x4400
	v_writelane_b32 v254, s0, 2
	s_add_i32 s0, 0, 0x14400
	v_writelane_b32 v254, s0, 3
	s_add_i32 s0, 0, 0x20840
	v_writelane_b32 v254, s0, 4
	s_add_i32 s0, 0, 0x21400
	v_writelane_b32 v254, s0, 5
	s_add_i32 s0, 0, 0x23000
	v_writelane_b32 v254, s0, 6
	s_add_i32 s0, 0, 0x23400
	v_writelane_b32 v254, s0, 7
	s_add_i32 s0, 0, 0x21800
	v_writelane_b32 v254, s0, 8
	s_add_i32 s0, 0, 0x21c00
	v_writelane_b32 v254, s0, 9
	s_add_i32 s0, 0, 0x23800
	v_writelane_b32 v254, s0, 10
	s_add_i32 s0, 0, 0x23c00
	v_writelane_b32 v254, s0, 11
	s_add_i32 s0, 0, 0x22000
	v_writelane_b32 v254, s0, 12
	s_add_i32 s0, 0, 0x22400
	v_writelane_b32 v254, s0, 13
	s_add_i32 s0, 0, 0x24000
	v_writelane_b32 v254, s0, 14
	s_add_i32 s0, 0, 0x24400
	v_writelane_b32 v254, s0, 15
	s_add_i32 s0, 0, 0x22800
	v_writelane_b32 v254, s0, 16
	s_add_i32 s0, 0, 0x22c00
	v_writelane_b32 v254, s0, 17
	s_add_i32 s0, 0, 0x24800
	v_writelane_b32 v254, s0, 18
	s_add_i32 s0, 0, 0x24c00
	v_writelane_b32 v254, s0, 19
	s_mov_b32 s1, 0
	s_mov_b32 s0, s8
	v_writelane_b32 v254, s0, 20
	s_ashr_i32 s7, s6, 31
	s_movk_i32 s3, 0x90
	v_writelane_b32 v254, s1, 21
	v_writelane_b32 v254, s4, 22
	s_mov_b32 s0, s6
	v_mov_b32_e32 v193, 0x8000
	v_writelane_b32 v254, s5, 23
	v_writelane_b32 v254, s0, 24
	s_lshl_b64 s[4:5], s[6:7], 18
	v_mbcnt_hi_u32_b32 v195, -1, v0
	v_writelane_b32 v254, s1, 25
	v_writelane_b32 v254, s4, 26
	v_mov_b32_e32 v196, 0x2200
	v_mov_b32_e32 v197, 0x80
	v_writelane_b32 v254, s5, 27
	v_writelane_b32 v254, s2, 28
	v_writelane_b32 v254, s90, 29
	v_mov_b32_e32 v198, 0xf149f2ca
	v_mov_b32_e32 v199, 0x41b17218
	v_writelane_b32 v254, s91, 30
	v_writelane_b32 v254, s92, 31
	v_mov_b32_e32 v200, 0x200
	v_mov_b64_e32 v[140:141], 0x200
	v_writelane_b32 v254, s93, 32
	v_writelane_b32 v254, s94, 33
	v_writelane_b32 v254, s95, 34
	s_mov_b32 s33, 0x6040200
	s_mov_b32 s76, 0x7050301
	s_mov_b32 s77, 0x3d800000
	s_movk_i32 s72, 0x220
	s_mov_b32 s78, 0x7f800000
	s_movk_i32 s83, 0x3200
	s_movk_i32 s84, 0x5ff
	s_movk_i32 s85, 0x110
	s_movk_i32 s87, 0x210
	s_mov_b32 s88, 0xf800000
	s_add_i32 s89, 0, 0x20800
	s_add_i32 s86, 0, 0x25010
	s_add_i32 s81, 0, 0x25020
	s_add_i32 s23, 0, 0x25030
	s_mov_b64 s[24:25], 0x80
	s_mov_b64 s[26:27], 0x200
	s_mov_b32 s34, 0x3b0293ee
	s_mov_b32 s16, 0x3db504f3
	s_waitcnt lgkmcnt(0)
	s_mov_b64 s[18:19], 0x1000000
	s_mov_b32 s20, 0x3fd744fd
	s_mov_b32 s22, 0x3e800000
	s_mov_b32 s5, 0
	v_writelane_b32 v254, s80, 35
	s_branch .LBB0_146

.LBB0_545:
	v_add_u32_e32 v205, v167, v176
	v_lshlrev_b32_e32 v206, 1, v160
	s_waitcnt vmcnt(15)
	ds_write_b128 v205, v[0:3]
	s_waitcnt vmcnt(14)
	ds_write_b128 v205, v[4:7] offset:1152
	s_waitcnt vmcnt(13)
	ds_write_b128 v205, v[8:11] offset:2304
	s_waitcnt vmcnt(12)
	ds_write_b128 v205, v[12:15] offset:3456
	v_add_u32_e32 v224, s60, v206
	ds_read_u16 v0, v224 offset:256
	ds_read_u16 v1, v224 offset:272
	ds_read_u16 v2, v224 offset:288
	ds_read_u16 v3, v224 offset:304
	s_cmp_gt_i32 s63, 2
	s_waitcnt lgkmcnt(3)
	v_lshl_or_b32 v0, v0, 9, v182
	s_waitcnt lgkmcnt(2)
	v_lshl_or_b32 v1, v1, 9, v182
	global_load_dwordx4 v[8:11], v0, s[48:49]
	global_load_dwordx4 v[64:67], v1, s[48:49]
	s_waitcnt lgkmcnt(1)
	v_lshl_or_b32 v0, v2, 9, v182
	s_waitcnt lgkmcnt(0)
	v_lshl_or_b32 v1, v3, 9, v182
	global_load_dwordx4 v[68:71], v0, s[48:49]
	global_load_dwordx4 v[4:7], v1, s[48:49]
	s_cselect_b64 s[8:9], -1, 0
	s_cmp_lt_i32 s29, s31
	s_cselect_b64 s[0:1], -1, 0
	s_add_i32 s64, s63, 1
	s_add_i32 s21, s64, s58
	s_cmp_lt_i32 s63, 3
	s_cselect_b64 s[6:7], -1, 0
	s_and_b64 s[10:11], s[6:7], exec
	s_cselect_b32 s10, s21, s29
	s_sub_i32 s62, s59, s10
	s_or_b64 s[0:1], s[6:7], s[0:1]
	s_and_b64 s[6:7], s[0:1], exec
	s_cselect_b32 s10, s62, s56
	s_ashr_i32 s11, s10, 31
	s_lshl_b64 s[6:7], s[10:11], 9
	v_lshl_add_u64 v[0:1], v[144:145], 0, s[6:7]
	v_add_u32_e32 v116, 0x800, v179
	global_load_ushort v117, v[0:1], off
	global_load_ushort v118, v[0:1], off offset:128
	global_load_ushort v119, v[0:1], off offset:256
	global_load_ushort v120, v[0:1], off offset:384
	ds_read2_b64 v[0:3], v116 offset0:32 offset1:36
	ds_read2_b64 v[12:15], v179 offset1:4
	s_waitcnt vmcnt(17) lgkmcnt(1)
	v_mfma_f32_16x16x32_fp8_fp8 v[76:79], v[0:1], v[154:155], 0
	s_waitcnt lgkmcnt(0)
	v_mfma_f32_16x16x32_fp8_fp8 v[72:75], v[12:13], v[154:155], 0
	v_mfma_f32_16x16x32_fp8_fp8 v[12:15], v[14:15], v[152:153], v[72:75]
	v_mfma_f32_16x16x32_fp8_fp8 v[0:3], v[2:3], v[152:153], v[76:79]
	s_nop 5
	ds_read2_b64 v[72:75], v179 offset0:8 offset1:12
	ds_read2_b64 v[76:79], v116 offset0:40 offset1:44
	s_waitcnt vmcnt(19)
	ds_write_b128 v205, v[28:31] offset:9216
	s_waitcnt vmcnt(18)
	ds_write_b128 v205, v[16:19] offset:10368
	s_waitcnt vmcnt(17)
	ds_write_b128 v205, v[20:23] offset:11520
	s_waitcnt vmcnt(16)
	ds_write_b128 v205, v[24:27] offset:12672
	ds_read_u16 v16, v224 offset:320
	ds_read_u16 v17, v224 offset:336
	ds_read_u16 v18, v224 offset:352
	ds_read_u16 v19, v224 offset:368
	s_waitcnt lgkmcnt(9)
	v_mfma_f32_16x16x32_fp8_fp8 v[12:15], v[72:73], v[148:149], v[12:15]
	s_waitcnt lgkmcnt(3)
	v_lshl_or_b32 v16, v16, 9, v182
	global_load_dwordx4 v[20:23], v16, s[48:49]
	s_waitcnt lgkmcnt(2)
	v_lshl_or_b32 v16, v17, 9, v182
	global_load_dwordx4 v[28:31], v16, s[48:49]
	s_waitcnt lgkmcnt(1)
	v_lshl_or_b32 v16, v18, 9, v182
	global_load_dwordx4 v[24:27], v16, s[48:49]
	s_waitcnt lgkmcnt(0)
	v_lshl_or_b32 v16, v19, 9, v182
	global_load_dwordx4 v[88:91], v16, s[48:49]
	v_mfma_f32_16x16x32_fp8_fp8 v[0:3], v[76:77], v[148:149], v[0:3]
	v_mfma_f32_16x16x32_fp8_fp8 v[12:15], v[74:75], v[150:151], v[12:15]
	v_mfma_f32_16x16x32_fp8_fp8 v[0:3], v[78:79], v[150:151], v[0:3]
	v_add_u32_e32 v124, 0x2800, v179
	v_add_u32_e32 v125, 0x2000, v179
	ds_read2_b64 v[16:19], v124 offset0:160 offset1:164
	ds_read2_b64 v[72:75], v125 offset0:128 offset1:132
	s_waitcnt lgkmcnt(0)
	v_mfma_f32_16x16x32_fp8_fp8 v[76:79], v[72:73], v[154:155], 0
	v_mfma_f32_16x16x32_fp8_fp8 v[80:83], v[16:17], v[154:155], 0
	v_mfma_f32_16x16x32_fp8_fp8 v[72:75], v[74:75], v[152:153], v[76:79]
	v_mfma_f32_16x16x32_fp8_fp8 v[16:19], v[18:19], v[152:153], v[80:83]
	s_nop 4
	ds_read2_b64 v[76:79], v125 offset0:136 offset1:140
	ds_read2_b64 v[80:83], v124 offset0:168 offset1:172
	s_waitcnt vmcnt(19)
	ds_write_b128 v205, v[48:51]
	s_waitcnt vmcnt(18)
	ds_write_b128 v205, v[52:55] offset:1152
	s_waitcnt vmcnt(17)
	ds_write_b128 v205, v[56:59] offset:2304
	s_waitcnt vmcnt(16)
	ds_write_b128 v205, v[60:63] offset:3456
	ds_read_u16 v48, v224 offset:384
	ds_read_u16 v52, v224 offset:400
	ds_read_u16 v56, v224 offset:416
	ds_read_u16 v60, v224 offset:432
	s_waitcnt lgkmcnt(8)
	v_mfma_f32_16x16x32_fp8_fp8 v[16:19], v[80:81], v[148:149], v[16:19]
	s_waitcnt lgkmcnt(3)
	v_lshl_or_b32 v48, v48, 9, v182
	s_waitcnt lgkmcnt(2)
	v_lshl_or_b32 v52, v52, 9, v182
	s_waitcnt lgkmcnt(1)
	v_lshl_or_b32 v56, v56, 9, v182
	s_waitcnt lgkmcnt(0)
	v_lshl_or_b32 v60, v60, 9, v182
	global_load_dwordx4 v[48:51], v48, s[48:49]
	v_mfma_f32_16x16x32_fp8_fp8 v[72:75], v[76:77], v[148:149], v[72:75]
	global_load_dwordx4 v[52:55], v52, s[48:49]
	s_nop 0
	global_load_dwordx4 v[56:59], v56, s[48:49]
	v_mfma_f32_16x16x32_fp8_fp8 v[16:19], v[82:83], v[150:151], v[16:19]
	global_load_dwordx4 v[60:63], v60, s[48:49]
	v_mfma_f32_16x16x32_fp8_fp8 v[72:75], v[78:79], v[150:151], v[72:75]
	ds_read2_b64 v[76:79], v116 offset0:32 offset1:36
	ds_read2_b64 v[80:83], v179 offset1:4
	s_waitcnt lgkmcnt(1)
	v_mfma_f32_16x16x32_fp8_fp8 v[92:95], v[76:77], v[154:155], 0
	s_waitcnt lgkmcnt(0)
	v_mfma_f32_16x16x32_fp8_fp8 v[84:87], v[80:81], v[154:155], 0
	v_mfma_f32_16x16x32_fp8_fp8 v[80:83], v[82:83], v[152:153], v[84:87]
	v_mfma_f32_16x16x32_fp8_fp8 v[76:79], v[78:79], v[152:153], v[92:95]
	s_nop 5
	ds_read2_b64 v[84:87], v179 offset0:8 offset1:12
	ds_read2_b64 v[92:95], v116 offset0:40 offset1:44
	s_waitcnt vmcnt(19)
	ds_write_b128 v205, v[32:35] offset:9216
	s_waitcnt vmcnt(18)
	ds_write_b128 v205, v[36:39] offset:10368
	s_waitcnt vmcnt(17)
	ds_write_b128 v205, v[40:43] offset:11520
	s_waitcnt vmcnt(16)
	ds_write_b128 v205, v[44:47] offset:12672
	ds_read_u16 v32, v224 offset:448
	ds_read_u16 v36, v224 offset:464
	ds_read_u16 v40, v224 offset:480
	ds_read_u16 v44, v224 offset:496
	s_waitcnt lgkmcnt(9)
	v_mfma_f32_16x16x32_fp8_fp8 v[80:83], v[84:85], v[148:149], v[80:83]
	s_waitcnt lgkmcnt(3)
	v_lshl_or_b32 v32, v32, 9, v182
	s_waitcnt lgkmcnt(2)
	v_lshl_or_b32 v36, v36, 9, v182
	s_waitcnt lgkmcnt(1)
	v_lshl_or_b32 v40, v40, 9, v182
	s_waitcnt lgkmcnt(0)
	v_lshl_or_b32 v44, v44, 9, v182
	global_load_dwordx4 v[32:35], v32, s[48:49]
	v_mfma_f32_16x16x32_fp8_fp8 v[76:79], v[92:93], v[148:149], v[76:79]
	global_load_dwordx4 v[36:39], v36, s[48:49]
	s_nop 0
	global_load_dwordx4 v[40:43], v40, s[48:49]
	v_mfma_f32_16x16x32_fp8_fp8 v[84:87], v[86:87], v[150:151], v[80:83]
	global_load_dwordx4 v[44:47], v44, s[48:49]
	v_mfma_f32_16x16x32_fp8_fp8 v[80:83], v[94:95], v[150:151], v[76:79]
	s_nop 2
	ds_read2_b64 v[76:79], v124 offset0:160 offset1:164
	ds_read2_b64 v[92:95], v125 offset0:128 offset1:132
	s_waitcnt lgkmcnt(1)
	v_mfma_f32_16x16x32_fp8_fp8 v[100:103], v[76:77], v[154:155], 0
	s_waitcnt lgkmcnt(0)
	v_mfma_f32_16x16x32_fp8_fp8 v[96:99], v[92:93], v[154:155], 0
	v_mfma_f32_16x16x32_fp8_fp8 v[92:95], v[94:95], v[152:153], v[96:99]
	v_mfma_f32_16x16x32_fp8_fp8 v[76:79], v[78:79], v[152:153], v[100:103]
	s_nop 5
	ds_read2_b64 v[96:99], v125 offset0:136 offset1:140
	ds_read2_b64 v[100:103], v124 offset0:168 offset1:172
	s_waitcnt vmcnt(19)
	ds_write_b128 v205, v[8:11]
	s_waitcnt vmcnt(18)
	ds_write_b128 v205, v[64:67] offset:1152
	s_waitcnt vmcnt(17)
	ds_write_b128 v205, v[68:71] offset:2304
	s_waitcnt vmcnt(16)
	ds_write_b128 v205, v[4:7] offset:3456
	ds_read_u16 v4, v224
	ds_read_u16 v8, v224 offset:16
	ds_read_u16 v64, v224 offset:32
	ds_read_u16 v65, v224 offset:48
	s_waitcnt lgkmcnt(9)
	v_mfma_f32_16x16x32_fp8_fp8 v[92:95], v[96:97], v[148:149], v[92:95]
	s_waitcnt lgkmcnt(3)
	v_lshl_or_b32 v4, v4, 9, v182
	s_waitcnt lgkmcnt(2)
	v_lshl_or_b32 v8, v8, 9, v182
	s_waitcnt lgkmcnt(1)
	v_lshl_or_b32 v64, v64, 9, v182
	v_mfma_f32_16x16x32_fp8_fp8 v[76:79], v[100:101], v[148:149], v[76:79]
	global_load_dwordx4 v[4:7], v4, s[50:51]
	s_nop 0
	global_load_dwordx4 v[8:11], v8, s[50:51]
	v_mfma_f32_16x16x32_fp8_fp8 v[96:99], v[98:99], v[150:151], v[92:95]
	global_load_dwordx4 v[68:71], v64, s[50:51]
	s_waitcnt lgkmcnt(0)
	v_lshl_or_b32 v64, v65, 9, v182
	v_mfma_f32_16x16x32_fp8_fp8 v[92:95], v[102:103], v[150:151], v[76:79]
	s_nop 2
	global_load_dwordx4 v[76:79], v64, s[50:51]
	ds_read2_b64 v[64:67], v116 offset0:32 offset1:36
	ds_read2_b64 v[100:103], v179 offset1:4
	s_waitcnt lgkmcnt(1)
	v_mfma_f32_16x16x32_fp8_fp8 v[108:111], v[64:65], v[154:155], 0
	s_waitcnt lgkmcnt(0)
	v_mfma_f32_16x16x32_fp8_fp8 v[104:107], v[100:101], v[154:155], 0
	v_mfma_f32_16x16x32_fp8_fp8 v[100:103], v[102:103], v[152:153], v[104:107]
	v_mfma_f32_16x16x32_fp8_fp8 v[64:67], v[66:67], v[152:153], v[108:111]
	s_nop 5
	ds_read2_b64 v[104:107], v179 offset0:8 offset1:12
	ds_read2_b64 v[108:111], v116 offset0:40 offset1:44
	s_waitcnt vmcnt(15)
	ds_write_b128 v205, v[20:23] offset:9216
	s_waitcnt vmcnt(14)
	ds_write_b128 v205, v[28:31] offset:10368
	s_waitcnt vmcnt(13)
	ds_write_b128 v205, v[24:27] offset:11520
	s_waitcnt vmcnt(12)
	ds_write_b128 v205, v[88:91] offset:12672
	s_waitcnt lgkmcnt(5)
	v_mfma_f32_16x16x32_fp8_fp8 v[100:103], v[104:105], v[148:149], v[100:103]
	s_waitcnt lgkmcnt(4)
	v_mfma_f32_16x16x32_fp8_fp8 v[64:67], v[108:109], v[148:149], v[64:67]
	v_mfma_f32_16x16x32_fp8_fp8 v[104:107], v[106:107], v[150:151], v[100:103]
	v_mfma_f32_16x16x32_fp8_fp8 v[100:103], v[110:111], v[150:151], v[64:67]
	ds_read_u16 v20, v224 offset:64
	ds_read_u16 v24, v224 offset:80
	ds_read_u16 v28, v224 offset:96
	s_nop 2
	ds_read_u16 v64, v224 offset:112
	s_waitcnt lgkmcnt(3)
	v_lshl_or_b32 v20, v20, 9, v182
	s_waitcnt lgkmcnt(2)
	v_lshl_or_b32 v24, v24, 9, v182
	s_waitcnt lgkmcnt(1)
	v_lshl_or_b32 v28, v28, 9, v182
	s_waitcnt lgkmcnt(0)
	v_lshl_or_b32 v64, v64, 9, v182
	global_load_dwordx4 v[20:23], v20, s[50:51]
	s_nop 0
	global_load_dwordx4 v[24:27], v24, s[50:51]
	s_nop 0
	global_load_dwordx4 v[28:31], v28, s[50:51]
	s_nop 0
	global_load_dwordx4 v[64:67], v64, s[50:51]
	ds_read2_b64 v[88:91], v124 offset0:160 offset1:164
	ds_read2_b64 v[108:111], v125 offset0:128 offset1:132
	s_waitcnt lgkmcnt(1)
	v_mfma_f32_16x16x32_fp8_fp8 v[126:129], v[88:89], v[154:155], 0
	s_waitcnt lgkmcnt(0)
	v_mfma_f32_16x16x32_fp8_fp8 v[112:115], v[108:109], v[154:155], 0
	v_mfma_f32_16x16x32_fp8_fp8 v[108:111], v[110:111], v[152:153], v[112:115]
	v_mfma_f32_16x16x32_fp8_fp8 v[88:91], v[90:91], v[152:153], v[126:129]
	s_nop 5
	ds_read2_b64 v[112:115], v125 offset0:136 offset1:140
	ds_read2_b64 v[126:129], v124 offset0:168 offset1:172
	s_waitcnt vmcnt(15)
	ds_write_b128 v205, v[48:51]
	s_waitcnt vmcnt(14)
	ds_write_b128 v205, v[52:55] offset:1152
	s_waitcnt vmcnt(13)
	ds_write_b128 v205, v[56:59] offset:2304
	s_waitcnt vmcnt(12)
	ds_write_b128 v205, v[60:63] offset:3456
	ds_read_u16 v48, v224 offset:128
	ds_read_u16 v52, v224 offset:144
	ds_read_u16 v56, v224 offset:160
	ds_read_u16 v60, v224 offset:176
	s_waitcnt lgkmcnt(9)
	v_mfma_f32_16x16x32_fp8_fp8 v[108:111], v[112:113], v[148:149], v[108:111]
	s_waitcnt lgkmcnt(3)
	v_lshl_or_b32 v48, v48, 9, v182
	s_waitcnt lgkmcnt(2)
	v_lshl_or_b32 v52, v52, 9, v182
	s_waitcnt lgkmcnt(1)
	v_lshl_or_b32 v56, v56, 9, v182
	s_waitcnt lgkmcnt(0)
	v_lshl_or_b32 v60, v60, 9, v182
	global_load_dwordx4 v[48:51], v48, s[50:51]
	v_mfma_f32_16x16x32_fp8_fp8 v[88:91], v[126:127], v[148:149], v[88:91]
	global_load_dwordx4 v[52:55], v52, s[50:51]
	s_nop 0
	global_load_dwordx4 v[56:59], v56, s[50:51]
	v_mfma_f32_16x16x32_fp8_fp8 v[112:115], v[114:115], v[150:151], v[108:111]
	global_load_dwordx4 v[60:63], v60, s[50:51]
	v_mfma_f32_16x16x32_fp8_fp8 v[108:111], v[128:129], v[150:151], v[88:91]
	s_nop 2
	v_lshl_add_u32 v88, v142, 1, s61
	ds_write_b16 v88, v117
	ds_write_b16 v88, v118 offset:128
	ds_write_b16 v88, v119 offset:256
	ds_write_b16 v88, v120 offset:384
	ds_read2_b64 v[88:91], v116 offset0:32 offset1:36
	ds_read2_b64 v[118:121], v179 offset1:4
	s_waitcnt lgkmcnt(1)
	v_mfma_f32_16x16x32_fp8_fp8 v[130:133], v[88:89], v[154:155], 0
	s_waitcnt lgkmcnt(0)
	v_mfma_f32_16x16x32_fp8_fp8 v[126:129], v[118:119], v[154:155], 0
	v_mfma_f32_16x16x32_fp8_fp8 v[118:121], v[120:121], v[152:153], v[126:129]
	v_mfma_f32_16x16x32_fp8_fp8 v[88:91], v[90:91], v[152:153], v[130:133]
	s_nop 5
	ds_read2_b64 v[126:129], v179 offset0:8 offset1:12
	ds_read2_b64 v[130:133], v116 offset0:40 offset1:44
	s_waitcnt vmcnt(15)
	ds_write_b128 v205, v[32:35] offset:9216
	s_waitcnt vmcnt(14)
	ds_write_b128 v205, v[36:39] offset:10368
	s_waitcnt vmcnt(13)
	ds_write_b128 v205, v[40:43] offset:11520
	s_waitcnt vmcnt(12)
	ds_write_b128 v205, v[44:47] offset:12672
	ds_read_u16 v32, v224 offset:192
	ds_read_u16 v36, v224 offset:208
	ds_read_u16 v40, v224 offset:224
	ds_read_u16 v44, v224 offset:240
	s_waitcnt lgkmcnt(9)
	v_mfma_f32_16x16x32_fp8_fp8 v[116:119], v[126:127], v[148:149], v[118:121]
	s_waitcnt lgkmcnt(3)
	v_lshl_or_b32 v32, v32, 9, v182
	s_waitcnt lgkmcnt(2)
	v_lshl_or_b32 v36, v36, 9, v182
	s_waitcnt lgkmcnt(1)
	v_lshl_or_b32 v40, v40, 9, v182
	s_waitcnt lgkmcnt(0)
	v_lshl_or_b32 v44, v44, 9, v182
	global_load_dwordx4 v[32:35], v32, s[50:51]
	v_mfma_f32_16x16x32_fp8_fp8 v[88:91], v[130:131], v[148:149], v[88:91]
	global_load_dwordx4 v[36:39], v36, s[50:51]
	s_nop 0
	global_load_dwordx4 v[40:43], v40, s[50:51]
	v_mfma_f32_16x16x32_fp8_fp8 v[120:123], v[128:129], v[150:151], v[116:119]
	global_load_dwordx4 v[44:47], v44, s[50:51]
	v_mfma_f32_16x16x32_fp8_fp8 v[116:119], v[132:133], v[150:151], v[88:91]
	s_nop 2
	ds_read2_b64 v[88:91], v124 offset0:160 offset1:164
	ds_read2_b64 v[126:129], v125 offset0:128 offset1:132
	s_waitcnt lgkmcnt(1)
	v_mfma_f32_16x16x32_fp8_fp8 v[208:211], v[88:89], v[154:155], 0
	s_waitcnt lgkmcnt(0)
	v_mfma_f32_16x16x32_fp8_fp8 v[130:133], v[126:127], v[154:155], 0
	v_mfma_f32_16x16x32_fp8_fp8 v[126:129], v[128:129], v[152:153], v[130:133]
	v_mfma_f32_16x16x32_fp8_fp8 v[88:91], v[90:91], v[152:153], v[208:211]
	s_nop 5
	ds_read2_b64 v[130:133], v125 offset0:136 offset1:140
	ds_read2_b64 v[208:211], v124 offset0:168 offset1:172
	s_waitcnt lgkmcnt(0)
	v_mfma_f32_16x16x32_fp8_fp8 v[88:91], v[208:209], v[148:149], v[88:91]
	v_mfma_f32_16x16x32_fp8_fp8 v[124:127], v[130:131], v[148:149], v[126:129]
	v_mfma_f32_16x16x32_fp8_fp8 v[128:131], v[210:211], v[150:151], v[88:91]
	s_nop 5
	v_max3_f32 v88, v12, s17, v13
	v_max3_f32 v88, v88, v14, v15
	v_max3_f32 v88, v88, v0, v1
	v_max3_f32 v88, v88, v2, v3
	v_max3_f32 v88, v88, v72, v73
	v_max3_f32 v88, v88, v74, v75
	v_max3_f32 v88, v88, v16, v17
	v_max3_f32 v88, v88, v18, v19
	v_max3_f32 v88, v88, v84, v85
	v_max3_f32 v88, v88, v86, v87
	v_max3_f32 v88, v88, v80, v81
	v_max3_f32 v88, v88, v82, v83
	v_max3_f32 v88, v88, v96, v97
	v_max3_f32 v88, v88, v98, v99
	v_max3_f32 v88, v88, v92, v93
	v_max3_f32 v88, v88, v94, v95
	v_max3_f32 v88, v88, v104, v105
	v_max3_f32 v88, v88, v106, v107
	v_max3_f32 v88, v88, v100, v101
	v_max3_f32 v88, v88, v102, v103
	v_max3_f32 v88, v88, v112, v113
	v_max3_f32 v88, v88, v114, v115
	v_max3_f32 v88, v88, v108, v109
	v_max3_f32 v88, v88, v110, v111
	v_mfma_f32_16x16x32_fp8_fp8 v[132:135], v[132:133], v[150:151], v[124:127]
	v_max3_f32 v88, v88, v120, v121
	v_max3_f32 v88, v88, v122, v123
	v_max3_f32 v88, v88, v116, v117
	v_max3_f32 v88, v88, v118, v119
	s_nop 3
	v_max3_f32 v88, v88, v132, v133
	v_max3_f32 v88, v88, v134, v135
	v_max3_f32 v88, v88, v128, v129
	v_max3_f32 v88, v88, v130, v131
	ds_bpermute_b32 v89, v184, v88
	s_waitcnt lgkmcnt(0)
	v_max_f32_e32 v89, v89, v89
	v_max_f32_e32 v88, v88, v89
	ds_bpermute_b32 v89, v185, v88
	s_waitcnt lgkmcnt(0)
	v_max_f32_e32 v89, v89, v89
	v_max_f32_e32 v89, v88, v89
	v_mov_b32_e32 v88, v3
	v_pk_mul_f32 v[158:159], v[88:89], s[34:35] op_sel_hi:[1,0]
	s_nop 0
	v_fma_f32 v3, v12, s34, -v159
	v_fma_f32 v13, v13, s34, -v159
	v_exp_f32_e32 v3, v3
	v_fma_f32 v14, v14, s34, -v159
	v_exp_f32_e32 v13, v13
	v_fma_f32 v15, v15, s34, -v159
	v_exp_f32_e32 v14, v14
	v_fma_f32 v0, v0, s34, -v159
	v_exp_f32_e32 v15, v15
	v_fma_f32 v1, v1, s34, -v159
	v_add_f32_e32 v12, 0, v3
	v_exp_f32_e32 v0, v0
	v_fma_f32 v2, v2, s34, -v159
	v_add_f32_e32 v12, v13, v12
	v_exp_f32_e32 v1, v1
	v_sub_f32_e32 v88, v158, v159
	v_add_f32_e32 v12, v14, v12
	v_exp_f32_e32 v2, v2
	v_add_f32_e32 v12, v15, v12
	v_exp_f32_e32 v88, v88
	v_add_f32_e32 v12, v0, v12
	v_add_f32_e32 v12, v1, v12
	v_add_f32_e32 v12, v2, v12
	v_add_f32_e32 v12, v88, v12
	v_cvt_pk_bf16_f32 v124, v3, v13
	v_cvt_pk_bf16_f32 v125, v14, v15
	v_cvt_pk_bf16_f32 v126, v0, v1
	v_cvt_pk_bf16_f32 v127, v2, v88
	v_fma_f32 v0, v72, s34, -v159
	v_fma_f32 v1, v73, s34, -v159
	v_exp_f32_e32 v0, v0
	v_fma_f32 v2, v74, s34, -v159
	v_exp_f32_e32 v1, v1
	v_fma_f32 v3, v75, s34, -v159
	v_exp_f32_e32 v2, v2
	v_fma_f32 v13, v16, s34, -v159
	v_exp_f32_e32 v3, v3
	v_fma_f32 v14, v17, s34, -v159
	v_add_f32_e32 v12, v0, v12
	v_exp_f32_e32 v13, v13
	v_fma_f32 v15, v18, s34, -v159
	v_add_f32_e32 v12, v1, v12
	v_exp_f32_e32 v14, v14
	v_fma_f32 v16, v19, s34, -v159
	v_add_f32_e32 v12, v2, v12
	v_exp_f32_e32 v15, v15
	v_add_f32_e32 v12, v3, v12
	v_exp_f32_e32 v16, v16
	v_add_f32_e32 v12, v13, v12
	v_add_f32_e32 v12, v14, v12
	v_add_f32_e32 v12, v15, v12
	v_add_f32_e32 v12, v16, v12
	v_cvt_pk_bf16_f32 v88, v0, v1
	v_cvt_pk_bf16_f32 v89, v2, v3
	v_cvt_pk_bf16_f32 v90, v13, v14
	v_cvt_pk_bf16_f32 v91, v15, v16
	v_fma_f32 v0, v84, s34, -v159
	v_fma_f32 v1, v85, s34, -v159
	v_exp_f32_e32 v0, v0
	v_fma_f32 v2, v86, s34, -v159
	v_exp_f32_e32 v1, v1
	v_fma_f32 v3, v87, s34, -v159
	v_exp_f32_e32 v2, v2
	v_fma_f32 v13, v80, s34, -v159
	v_exp_f32_e32 v3, v3
	v_fma_f32 v14, v81, s34, -v159
	v_add_f32_e32 v12, v0, v12
	v_exp_f32_e32 v13, v13
	v_fma_f32 v15, v82, s34, -v159
	v_add_f32_e32 v12, v1, v12
	v_exp_f32_e32 v14, v14
	v_fma_f32 v16, v83, s34, -v159
	v_add_f32_e32 v12, v2, v12
	v_exp_f32_e32 v15, v15
	v_add_f32_e32 v12, v3, v12
	v_exp_f32_e32 v16, v16
	v_add_f32_e32 v12, v13, v12
	v_add_f32_e32 v12, v14, v12
	v_add_f32_e32 v12, v15, v12
	v_add_f32_e32 v12, v16, v12
	v_cvt_pk_bf16_f32 v72, v0, v1
	v_cvt_pk_bf16_f32 v73, v2, v3
	v_cvt_pk_bf16_f32 v74, v13, v14
	v_cvt_pk_bf16_f32 v75, v15, v16
	v_fma_f32 v0, v96, s34, -v159
	v_fma_f32 v1, v97, s34, -v159
	v_exp_f32_e32 v0, v0
	v_fma_f32 v2, v98, s34, -v159
	v_exp_f32_e32 v1, v1
	v_fma_f32 v3, v99, s34, -v159
	v_exp_f32_e32 v2, v2
	v_fma_f32 v13, v92, s34, -v159
	v_exp_f32_e32 v3, v3
	v_fma_f32 v14, v93, s34, -v159
	v_add_f32_e32 v12, v0, v12
	v_exp_f32_e32 v13, v13
	v_fma_f32 v15, v94, s34, -v159
	v_add_f32_e32 v12, v1, v12
	v_exp_f32_e32 v14, v14
	v_fma_f32 v16, v95, s34, -v159
	v_add_f32_e32 v12, v2, v12
	v_exp_f32_e32 v15, v15
	v_add_f32_e32 v12, v3, v12
	v_exp_f32_e32 v16, v16
	v_add_f32_e32 v12, v13, v12
	v_add_f32_e32 v12, v14, v12
	v_add_f32_e32 v12, v15, v12
	v_add_f32_e32 v12, v16, v12
	v_cvt_pk_bf16_f32 v0, v0, v1
	v_cvt_pk_bf16_f32 v1, v2, v3
	v_cvt_pk_bf16_f32 v2, v13, v14
	v_cvt_pk_bf16_f32 v3, v15, v16
	v_fma_f32 v16, v107, s34, -v159
	v_fma_f32 v13, v104, s34, -v159
	v_fma_f32 v14, v105, s34, -v159
	v_exp_f32_e32 v17, v16
	v_fma_f32 v16, v100, s34, -v159
	v_exp_f32_e32 v13, v13
	v_fma_f32 v15, v106, s34, -v159
	v_exp_f32_e32 v14, v14
	v_exp_f32_e32 v18, v16
	v_fma_f32 v16, v101, s34, -v159
	v_exp_f32_e32 v15, v15
	v_exp_f32_e32 v19, v16
	v_fma_f32 v16, v102, s34, -v159
	v_add_f32_e32 v12, v13, v12
	v_add_f32_e32 v12, v14, v12
	v_exp_f32_e32 v80, v16
	v_fma_f32 v16, v103, s34, -v159
	v_add_f32_e32 v12, v15, v12
	v_add_f32_e32 v12, v17, v12
	v_exp_f32_e32 v81, v16
	v_add_f32_e32 v12, v18, v12
	v_add_f32_e32 v12, v19, v12
	v_add_f32_e32 v12, v80, v12
	v_add_f32_e32 v12, v81, v12
	v_cvt_pk_bf16_f32 v16, v13, v14
	v_cvt_pk_bf16_f32 v17, v15, v17
	v_cvt_pk_bf16_f32 v18, v18, v19
	v_cvt_pk_bf16_f32 v19, v80, v81
	v_fma_f32 v13, v112, s34, -v159
	v_exp_f32_e32 v158, v13
	v_fma_f32 v13, v113, s34, -v159
	v_exp_f32_e32 v207, v13
	v_fma_f32 v13, v114, s34, -v159
	v_exp_f32_e32 v208, v13
	v_fma_f32 v13, v115, s34, -v159
	v_exp_f32_e32 v209, v13
	v_fma_f32 v13, v108, s34, -v159
	v_exp_f32_e32 v210, v13
	v_fma_f32 v13, v109, s34, -v159
	v_exp_f32_e32 v211, v13
	v_fma_f32 v13, v110, s34, -v159
	v_add_f32_e32 v12, v158, v12
	v_add_f32_e32 v12, v207, v12
	v_exp_f32_e32 v212, v13
	v_fma_f32 v13, v111, s34, -v159
	v_add_f32_e32 v12, v208, v12
	v_add_f32_e32 v12, v209, v12
	v_exp_f32_e32 v213, v13
	v_add_f32_e32 v12, v210, v12
	v_add_f32_e32 v12, v211, v12
	v_add_f32_e32 v12, v212, v12
	v_add_f32_e32 v12, v213, v12
	v_fma_f32 v13, v120, s34, -v159
	v_exp_f32_e32 v214, v13
	v_fma_f32 v13, v121, s34, -v159
	v_exp_f32_e32 v215, v13
	v_fma_f32 v13, v122, s34, -v159
	v_exp_f32_e32 v216, v13
	v_fma_f32 v13, v123, s34, -v159
	v_exp_f32_e32 v217, v13
	v_fma_f32 v13, v116, s34, -v159
	v_exp_f32_e32 v218, v13
	v_fma_f32 v13, v117, s34, -v159
	v_exp_f32_e32 v219, v13
	v_fma_f32 v13, v118, s34, -v159
	v_add_f32_e32 v12, v214, v12
	v_add_f32_e32 v12, v215, v12
	v_exp_f32_e32 v220, v13
	v_fma_f32 v13, v119, s34, -v159
	v_add_f32_e32 v12, v216, v12
	v_add_f32_e32 v12, v217, v12
	v_exp_f32_e32 v221, v13
	v_add_f32_e32 v12, v218, v12
	v_add_f32_e32 v12, v219, v12
	v_add_f32_e32 v12, v220, v12
	v_add_f32_e32 v12, v221, v12
	v_fma_f32 v13, v132, s34, -v159
	v_exp_f32_e32 v222, v13
	v_fma_f32 v13, v133, s34, -v159
	v_exp_f32_e32 v223, v13
	v_fma_f32 v13, v134, s34, -v159
	v_exp_f32_e32 v134, v13
	v_fma_f32 v13, v135, s34, -v159
	v_exp_f32_e32 v135, v13
	v_fma_f32 v13, v128, s34, -v159
	v_exp_f32_e32 v128, v13
	v_fma_f32 v13, v129, s34, -v159
	v_exp_f32_e32 v129, v13
	v_fma_f32 v13, v130, s34, -v159
	v_add_f32_e32 v12, v222, v12
	v_add_f32_e32 v12, v223, v12
	v_exp_f32_e32 v130, v13
	v_fma_f32 v13, v131, s34, -v159
	v_add_f32_e32 v12, v134, v12
	v_add_f32_e32 v12, v135, v12
	v_exp_f32_e32 v131, v13
	v_add_f32_e32 v12, v128, v12
	v_add_f32_e32 v12, v129, v12
	v_add_f32_e32 v12, v130, v12
	v_add_f32_e32 v80, v131, v12
	s_waitcnt vmcnt(15)
	ds_write_b128 v205, v[4:7]
	s_waitcnt vmcnt(14)
	ds_write_b128 v205, v[8:11] offset:1152
	s_waitcnt vmcnt(13)
	ds_write_b128 v205, v[68:71] offset:2304
	s_waitcnt vmcnt(12)
	ds_write_b128 v205, v[76:79] offset:3456
	ds_read_u16 v4, v224 offset:256
	ds_read_u16 v5, v224 offset:272
	ds_read_u16 v12, v224 offset:288
	ds_read_u16 v13, v224 offset:304
	ds_bpermute_b32 v76, v184, v80
	s_waitcnt lgkmcnt(4)
	v_lshl_or_b32 v4, v4, 9, v182
	s_waitcnt lgkmcnt(3)
	v_lshl_or_b32 v8, v5, 9, v182
	s_waitcnt lgkmcnt(2)
	v_lshl_or_b32 v12, v12, 9, v182
	s_waitcnt lgkmcnt(1)
	v_lshl_or_b32 v68, v13, 9, v182
	global_load_dwordx4 v[4:7], v4, s[50:51]
	s_nop 0
	global_load_dwordx4 v[8:11], v8, s[50:51]
	s_nop 0
	global_load_dwordx4 v[12:15], v12, s[50:51]
	s_nop 0
	global_load_dwordx4 v[68:71], v68, s[50:51]
	s_waitcnt lgkmcnt(0)
	v_add_f32_e32 v132, v80, v76
	ds_bpermute_b32 v133, v185, v132
	ds_read_b64_tr_b16 v[76:77], v181
	ds_read_b64_tr_b16 v[84:85], v181 offset:32
	ds_read_b64_tr_b16 v[96:97], v181 offset:64
	ds_read_b64_tr_b16 v[104:105], v181 offset:96
	ds_read_b64_tr_b16 v[78:79], v181 offset:2304
	ds_read_b64_tr_b16 v[86:87], v181 offset:2336
	ds_read_b64_tr_b16 v[98:99], v181 offset:2368
	ds_read_b64_tr_b16 v[106:107], v181 offset:2400
	s_waitcnt vmcnt(15)
	ds_write_b128 v205, v[20:23] offset:9216
	s_waitcnt vmcnt(14)
	ds_write_b128 v205, v[24:27] offset:10368
	s_waitcnt vmcnt(13)
	ds_write_b128 v205, v[28:31] offset:11520
	s_waitcnt vmcnt(12)
	ds_write_b128 v205, v[64:67] offset:12672
	ds_read_u16 v20, v224 offset:320
	ds_read_u16 v21, v224 offset:336
	ds_read_u16 v28, v224 offset:352
	ds_read_u16 v29, v224 offset:368
	s_waitcnt lgkmcnt(14)
	v_perm_b32 v80, v77, v76, s33
	s_waitcnt lgkmcnt(3)
	v_lshl_or_b32 v20, v20, 9, v182
	s_waitcnt lgkmcnt(2)
	v_lshl_or_b32 v24, v21, 9, v182
	s_waitcnt lgkmcnt(1)
	v_lshl_or_b32 v28, v28, 9, v182
	s_waitcnt lgkmcnt(0)
	v_lshl_or_b32 v64, v29, 9, v182
	global_load_dwordx4 v[20:23], v20, s[50:51]
	s_nop 0
	global_load_dwordx4 v[24:27], v24, s[50:51]
	s_nop 0
	global_load_dwordx4 v[28:31], v28, s[50:51]
	s_nop 0
	global_load_dwordx4 v[64:67], v64, s[50:51]
	v_perm_b32 v81, v77, v76, s76
	v_perm_b32 v82, v79, v78, s33
	v_perm_b32 v83, v79, v78, s76
	v_perm_b32 v92, v85, v84, s33
	v_perm_b32 v93, v85, v84, s76
	v_perm_b32 v94, v87, v86, s33
	v_perm_b32 v95, v87, v86, s76
	v_perm_b32 v100, v97, v96, s33
	v_perm_b32 v101, v97, v96, s76
	v_perm_b32 v102, v99, v98, s33
	v_perm_b32 v103, v99, v98, s76
	v_perm_b32 v108, v105, v104, s33
	v_perm_b32 v109, v105, v104, s76
	v_perm_b32 v110, v107, v106, s33
	v_perm_b32 v111, v107, v106, s76
	v_cvt_scalef32_pk_bf16_fp8 v76, v80, 1.0
	v_cvt_scalef32_pk_bf16_fp8 v77, v80, 1.0 op_sel:[1,0,0]
	v_cvt_scalef32_pk_bf16_fp8 v78, v82, 1.0
	v_cvt_scalef32_pk_bf16_fp8 v79, v82, 1.0 op_sel:[1,0,0]
	v_cvt_scalef32_pk_bf16_fp8 v80, v81, 1.0
	v_cvt_scalef32_pk_bf16_fp8 v81, v81, 1.0 op_sel:[1,0,0]
	v_cvt_scalef32_pk_bf16_fp8 v82, v83, 1.0
	v_cvt_scalef32_pk_bf16_fp8 v83, v83, 1.0 op_sel:[1,0,0]
	v_cvt_scalef32_pk_bf16_fp8 v84, v92, 1.0
	v_cvt_scalef32_pk_bf16_fp8 v85, v92, 1.0 op_sel:[1,0,0]
	v_cvt_scalef32_pk_bf16_fp8 v86, v94, 1.0
	v_cvt_scalef32_pk_bf16_fp8 v87, v94, 1.0 op_sel:[1,0,0]
	v_cvt_scalef32_pk_bf16_fp8 v92, v93, 1.0
	v_cvt_scalef32_pk_bf16_fp8 v93, v93, 1.0 op_sel:[1,0,0]
	v_cvt_scalef32_pk_bf16_fp8 v94, v95, 1.0
	v_cvt_scalef32_pk_bf16_fp8 v95, v95, 1.0 op_sel:[1,0,0]
	v_cvt_scalef32_pk_bf16_fp8 v96, v100, 1.0
	v_cvt_scalef32_pk_bf16_fp8 v97, v100, 1.0 op_sel:[1,0,0]
	v_cvt_scalef32_pk_bf16_fp8 v98, v102, 1.0
	v_cvt_scalef32_pk_bf16_fp8 v99, v102, 1.0 op_sel:[1,0,0]
	v_cvt_scalef32_pk_bf16_fp8 v100, v101, 1.0
	v_cvt_scalef32_pk_bf16_fp8 v101, v101, 1.0 op_sel:[1,0,0]
	v_cvt_scalef32_pk_bf16_fp8 v102, v103, 1.0
	v_cvt_scalef32_pk_bf16_fp8 v103, v103, 1.0 op_sel:[1,0,0]
	v_cvt_scalef32_pk_bf16_fp8 v104, v108, 1.0
	v_cvt_scalef32_pk_bf16_fp8 v105, v108, 1.0 op_sel:[1,0,0]
	v_cvt_scalef32_pk_bf16_fp8 v106, v110, 1.0
	v_cvt_scalef32_pk_bf16_fp8 v107, v110, 1.0 op_sel:[1,0,0]
	v_cvt_scalef32_pk_bf16_fp8 v108, v109, 1.0
	v_cvt_scalef32_pk_bf16_fp8 v109, v109, 1.0 op_sel:[1,0,0]
	v_cvt_scalef32_pk_bf16_fp8 v110, v111, 1.0
	v_cvt_scalef32_pk_bf16_fp8 v111, v111, 1.0 op_sel:[1,0,0]
	v_mfma_f32_16x16x32_bf16 v[80:83], v[124:127], v[80:83], 0
	v_mfma_f32_16x16x32_bf16 v[92:95], v[124:127], v[92:95], 0
	v_mfma_f32_16x16x32_bf16 v[96:99], v[124:127], v[96:99], 0
	v_mfma_f32_16x16x32_bf16 v[100:103], v[124:127], v[100:103], 0
	v_mfma_f32_16x16x32_bf16 v[104:107], v[124:127], v[104:107], 0
	v_mfma_f32_16x16x32_bf16 v[108:111], v[124:127], v[108:111], 0
	v_mfma_f32_16x16x32_bf16 v[76:79], v[124:127], v[76:79], 0
	v_mfma_f32_16x16x32_bf16 v[84:87], v[124:127], v[84:87], 0
	ds_read_b64_tr_b16 v[112:113], v181 offset:11520
	ds_read_b64_tr_b16 v[114:115], v181 offset:9216
	ds_read_b64_tr_b16 v[120:121], v181 offset:9248
	s_waitcnt lgkmcnt(2)
	v_perm_b32 v119, v113, v112, s76
	s_waitcnt lgkmcnt(1)
	v_perm_b32 v116, v115, v114, s33
	v_perm_b32 v117, v115, v114, s76
	v_perm_b32 v115, v113, v112, s33
	v_cvt_scalef32_pk_bf16_fp8 v112, v116, 1.0
	v_cvt_scalef32_pk_bf16_fp8 v113, v116, 1.0 op_sel:[1,0,0]
	v_cvt_scalef32_pk_bf16_fp8 v114, v115, 1.0
	v_cvt_scalef32_pk_bf16_fp8 v115, v115, 1.0 op_sel:[1,0,0]
	v_cvt_scalef32_pk_bf16_fp8 v116, v117, 1.0
	v_cvt_scalef32_pk_bf16_fp8 v117, v117, 1.0 op_sel:[1,0,0]
	v_mfma_f32_16x16x32_bf16 v[76:79], v[88:91], v[112:115], v[76:79]
	ds_read_b64_tr_b16 v[112:113], v181 offset:11552
	v_cvt_scalef32_pk_bf16_fp8 v118, v119, 1.0
	v_cvt_scalef32_pk_bf16_fp8 v119, v119, 1.0 op_sel:[1,0,0]
	s_waitcnt lgkmcnt(1)
	v_perm_b32 v114, v121, v120, s33
	s_waitcnt lgkmcnt(0)
	v_perm_b32 v115, v113, v112, s33
	v_mfma_f32_16x16x32_bf16 v[80:83], v[88:91], v[116:119], v[80:83]
	v_perm_b32 v119, v113, v112, s76
	v_cvt_scalef32_pk_bf16_fp8 v112, v114, 1.0
	v_cvt_scalef32_pk_bf16_fp8 v113, v114, 1.0 op_sel:[1,0,0]
	v_cvt_scalef32_pk_bf16_fp8 v114, v115, 1.0
	v_cvt_scalef32_pk_bf16_fp8 v115, v115, 1.0 op_sel:[1,0,0]
	v_perm_b32 v117, v121, v120, s76
	v_cvt_scalef32_pk_bf16_fp8 v116, v117, 1.0
	v_mfma_f32_16x16x32_bf16 v[84:87], v[88:91], v[112:115], v[84:87]
	ds_read_b64_tr_b16 v[112:113], v181 offset:9280
	ds_read_b64_tr_b16 v[114:115], v181 offset:11584
	v_cvt_scalef32_pk_bf16_fp8 v117, v117, 1.0 op_sel:[1,0,0]
	v_cvt_scalef32_pk_bf16_fp8 v118, v119, 1.0
	v_cvt_scalef32_pk_bf16_fp8 v119, v119, 1.0 op_sel:[1,0,0]
	s_nop 1
	v_mfma_f32_16x16x32_bf16 v[92:95], v[88:91], v[116:119], v[92:95]
	s_waitcnt lgkmcnt(1)
	v_perm_b32 v116, v113, v112, s33
	s_waitcnt lgkmcnt(0)
	v_perm_b32 v118, v115, v114, s33
	v_perm_b32 v117, v113, v112, s76
	v_perm_b32 v119, v115, v114, s76
	v_cvt_scalef32_pk_bf16_fp8 v112, v116, 1.0
	v_cvt_scalef32_pk_bf16_fp8 v113, v116, 1.0 op_sel:[1,0,0]
	v_cvt_scalef32_pk_bf16_fp8 v114, v118, 1.0
	v_cvt_scalef32_pk_bf16_fp8 v115, v118, 1.0 op_sel:[1,0,0]
	v_cvt_scalef32_pk_bf16_fp8 v116, v117, 1.0
	v_cvt_scalef32_pk_bf16_fp8 v117, v117, 1.0 op_sel:[1,0,0]
	v_mfma_f32_16x16x32_bf16 v[96:99], v[88:91], v[112:115], v[96:99]
	ds_read_b64_tr_b16 v[112:113], v181 offset:9312
	ds_read_b64_tr_b16 v[114:115], v181 offset:11616
	s_waitcnt vmcnt(15)
	ds_write_b128 v205, v[48:51]
	s_waitcnt vmcnt(14)
	ds_write_b128 v205, v[52:55] offset:1152
	s_waitcnt vmcnt(13)
	ds_write_b128 v205, v[56:59] offset:2304
	s_waitcnt vmcnt(12)
	ds_write_b128 v205, v[60:63] offset:3456
	ds_read_u16 v48, v224 offset:384
	ds_read_u16 v52, v224 offset:400
	ds_read_u16 v56, v224 offset:416
	ds_read_u16 v60, v224 offset:432
	v_cvt_scalef32_pk_bf16_fp8 v118, v119, 1.0
	s_waitcnt lgkmcnt(3)
	v_lshl_or_b32 v48, v48, 9, v182
	s_waitcnt lgkmcnt(2)
	v_lshl_or_b32 v52, v52, 9, v182
	s_waitcnt lgkmcnt(1)
	v_lshl_or_b32 v56, v56, 9, v182
	s_waitcnt lgkmcnt(0)
	v_lshl_or_b32 v60, v60, 9, v182
	global_load_dwordx4 v[48:51], v48, s[50:51]
	v_cvt_scalef32_pk_bf16_fp8 v119, v119, 1.0 op_sel:[1,0,0]
	global_load_dwordx4 v[52:55], v52, s[50:51]
	s_nop 0
	global_load_dwordx4 v[56:59], v56, s[50:51]
	v_mfma_f32_16x16x32_bf16 v[100:103], v[88:91], v[116:119], v[100:103]
	global_load_dwordx4 v[60:63], v60, s[50:51]
	v_perm_b32 v116, v113, v112, s33
	v_perm_b32 v117, v113, v112, s76
	v_perm_b32 v118, v115, v114, s33
	v_perm_b32 v119, v115, v114, s76
	v_cvt_scalef32_pk_bf16_fp8 v112, v116, 1.0
	v_cvt_scalef32_pk_bf16_fp8 v113, v116, 1.0 op_sel:[1,0,0]
	v_cvt_scalef32_pk_bf16_fp8 v114, v118, 1.0
	v_cvt_scalef32_pk_bf16_fp8 v115, v118, 1.0 op_sel:[1,0,0]
	v_cvt_scalef32_pk_bf16_fp8 v116, v117, 1.0
	v_cvt_scalef32_pk_bf16_fp8 v117, v117, 1.0 op_sel:[1,0,0]
	v_cvt_scalef32_pk_bf16_fp8 v118, v119, 1.0
	v_cvt_scalef32_pk_bf16_fp8 v119, v119, 1.0 op_sel:[1,0,0]
	v_mfma_f32_16x16x32_bf16 v[104:107], v[88:91], v[112:115], v[104:107]
	s_nop 0
	v_mfma_f32_16x16x32_bf16 v[88:91], v[88:91], v[116:119], v[108:111]
	s_nop 2
	ds_read_b64_tr_b16 v[108:109], v181 offset:2304
	ds_read_b64_tr_b16 v[110:111], v181
	ds_read_b64_tr_b16 v[116:117], v181 offset:32
	s_waitcnt lgkmcnt(2)
	v_perm_b32 v115, v109, v108, s76
	s_waitcnt lgkmcnt(1)
	v_perm_b32 v112, v111, v110, s33
	v_perm_b32 v113, v111, v110, s76
	v_perm_b32 v111, v109, v108, s33
	v_cvt_scalef32_pk_bf16_fp8 v108, v112, 1.0
	v_cvt_scalef32_pk_bf16_fp8 v109, v112, 1.0 op_sel:[1,0,0]
	v_cvt_scalef32_pk_bf16_fp8 v110, v111, 1.0
	v_cvt_scalef32_pk_bf16_fp8 v111, v111, 1.0 op_sel:[1,0,0]
	v_cvt_scalef32_pk_bf16_fp8 v112, v113, 1.0
	v_cvt_scalef32_pk_bf16_fp8 v113, v113, 1.0 op_sel:[1,0,0]
	v_mfma_f32_16x16x32_bf16 v[76:79], v[72:75], v[108:111], v[76:79]
	ds_read_b64_tr_b16 v[108:109], v181 offset:2336
	v_cvt_scalef32_pk_bf16_fp8 v114, v115, 1.0
	v_cvt_scalef32_pk_bf16_fp8 v115, v115, 1.0 op_sel:[1,0,0]
	s_waitcnt lgkmcnt(1)
	v_perm_b32 v110, v117, v116, s33
	s_waitcnt lgkmcnt(0)
	v_perm_b32 v111, v109, v108, s33
	v_mfma_f32_16x16x32_bf16 v[80:83], v[72:75], v[112:115], v[80:83]
	v_perm_b32 v115, v109, v108, s76
	v_cvt_scalef32_pk_bf16_fp8 v108, v110, 1.0
	v_cvt_scalef32_pk_bf16_fp8 v109, v110, 1.0 op_sel:[1,0,0]
	v_cvt_scalef32_pk_bf16_fp8 v110, v111, 1.0
	v_cvt_scalef32_pk_bf16_fp8 v111, v111, 1.0 op_sel:[1,0,0]
	v_perm_b32 v113, v117, v116, s76
	v_cvt_scalef32_pk_bf16_fp8 v112, v113, 1.0
	v_mfma_f32_16x16x32_bf16 v[84:87], v[72:75], v[108:111], v[84:87]
	ds_read_b64_tr_b16 v[108:109], v181 offset:64
	ds_read_b64_tr_b16 v[110:111], v181 offset:2368
	v_cvt_scalef32_pk_bf16_fp8 v113, v113, 1.0 op_sel:[1,0,0]
	v_cvt_scalef32_pk_bf16_fp8 v114, v115, 1.0
	v_cvt_scalef32_pk_bf16_fp8 v115, v115, 1.0 op_sel:[1,0,0]
	s_nop 1
	v_mfma_f32_16x16x32_bf16 v[92:95], v[72:75], v[112:115], v[92:95]
	s_waitcnt lgkmcnt(1)
	v_perm_b32 v112, v109, v108, s33
	s_waitcnt lgkmcnt(0)
	v_perm_b32 v114, v111, v110, s33
	v_perm_b32 v113, v109, v108, s76
	v_perm_b32 v115, v111, v110, s76
	v_cvt_scalef32_pk_bf16_fp8 v108, v112, 1.0
	v_cvt_scalef32_pk_bf16_fp8 v109, v112, 1.0 op_sel:[1,0,0]
	v_cvt_scalef32_pk_bf16_fp8 v110, v114, 1.0
	v_cvt_scalef32_pk_bf16_fp8 v111, v114, 1.0 op_sel:[1,0,0]
	v_cvt_scalef32_pk_bf16_fp8 v112, v113, 1.0
	v_cvt_scalef32_pk_bf16_fp8 v113, v113, 1.0 op_sel:[1,0,0]
	v_mfma_f32_16x16x32_bf16 v[96:99], v[72:75], v[108:111], v[96:99]
	ds_read_b64_tr_b16 v[108:109], v181 offset:96
	ds_read_b64_tr_b16 v[110:111], v181 offset:2400
	s_waitcnt vmcnt(15)
	ds_write_b128 v205, v[32:35] offset:9216
	s_waitcnt vmcnt(14)
	ds_write_b128 v205, v[36:39] offset:10368
	s_waitcnt vmcnt(13)
	ds_write_b128 v205, v[40:43] offset:11520
	s_waitcnt vmcnt(12)
	ds_write_b128 v205, v[44:47] offset:12672
	ds_read_u16 v32, v224 offset:448
	ds_read_u16 v36, v224 offset:464
	ds_read_u16 v40, v224 offset:480
	ds_read_u16 v44, v224 offset:496
	v_cvt_scalef32_pk_bf16_fp8 v114, v115, 1.0
	s_waitcnt lgkmcnt(3)
	v_lshl_or_b32 v32, v32, 9, v182
	s_waitcnt lgkmcnt(2)
	v_lshl_or_b32 v36, v36, 9, v182
	s_waitcnt lgkmcnt(1)
	v_lshl_or_b32 v40, v40, 9, v182
	s_waitcnt lgkmcnt(0)
	v_lshl_or_b32 v44, v44, 9, v182
	global_load_dwordx4 v[32:35], v32, s[50:51]
	v_cvt_scalef32_pk_bf16_fp8 v115, v115, 1.0 op_sel:[1,0,0]
	global_load_dwordx4 v[36:39], v36, s[50:51]
	s_nop 0
	global_load_dwordx4 v[40:43], v40, s[50:51]
	v_mfma_f32_16x16x32_bf16 v[100:103], v[72:75], v[112:115], v[100:103]
	global_load_dwordx4 v[44:47], v44, s[50:51]
	v_perm_b32 v112, v109, v108, s33
	v_perm_b32 v113, v109, v108, s76
	v_perm_b32 v114, v111, v110, s33
	v_perm_b32 v115, v111, v110, s76
	v_cvt_scalef32_pk_bf16_fp8 v108, v112, 1.0
	v_cvt_scalef32_pk_bf16_fp8 v109, v112, 1.0 op_sel:[1,0,0]
	v_cvt_scalef32_pk_bf16_fp8 v110, v114, 1.0
	v_cvt_scalef32_pk_bf16_fp8 v111, v114, 1.0 op_sel:[1,0,0]
	v_cvt_scalef32_pk_bf16_fp8 v116, v113, 1.0
	v_cvt_scalef32_pk_bf16_fp8 v117, v113, 1.0 op_sel:[1,0,0]
	v_cvt_scalef32_pk_bf16_fp8 v118, v115, 1.0
	v_cvt_scalef32_pk_bf16_fp8 v119, v115, 1.0 op_sel:[1,0,0]
	v_mfma_f32_16x16x32_bf16 v[112:115], v[72:75], v[108:111], v[104:107]
	s_nop 0
	v_mfma_f32_16x16x32_bf16 v[88:91], v[72:75], v[116:119], v[88:91]
	ds_read_b64_tr_b16 v[72:73], v181 offset:11520
	ds_read_b64_tr_b16 v[74:75], v181 offset:9216
	ds_read_b64_tr_b16 v[108:109], v181 offset:9248
	v_add_u32_e32 v159, s61, v206
	s_waitcnt lgkmcnt(2)
	v_perm_b32 v107, v73, v72, s76
	s_waitcnt lgkmcnt(1)
	v_perm_b32 v104, v75, v74, s33
	v_perm_b32 v105, v75, v74, s76
	v_perm_b32 v75, v73, v72, s33
	v_cvt_scalef32_pk_bf16_fp8 v72, v104, 1.0
	v_cvt_scalef32_pk_bf16_fp8 v73, v104, 1.0 op_sel:[1,0,0]
	v_cvt_scalef32_pk_bf16_fp8 v74, v75, 1.0
	v_cvt_scalef32_pk_bf16_fp8 v75, v75, 1.0 op_sel:[1,0,0]
	v_cvt_scalef32_pk_bf16_fp8 v104, v105, 1.0
	v_cvt_scalef32_pk_bf16_fp8 v105, v105, 1.0 op_sel:[1,0,0]
	v_cvt_scalef32_pk_bf16_fp8 v106, v107, 1.0
	v_cvt_scalef32_pk_bf16_fp8 v107, v107, 1.0 op_sel:[1,0,0]
	v_mfma_f32_16x16x32_bf16 v[72:75], v[0:3], v[72:75], v[76:79]
	s_nop 0
	v_mfma_f32_16x16x32_bf16 v[76:79], v[0:3], v[104:107], v[80:83]
	s_waitcnt lgkmcnt(0)
	v_perm_b32 v105, v109, v108, s76
	v_cvt_scalef32_pk_bf16_fp8 v104, v105, 1.0
	v_cvt_scalef32_pk_bf16_fp8 v105, v105, 1.0 op_sel:[1,0,0]
	ds_read_b64_tr_b16 v[80:81], v181 offset:11552
	v_perm_b32 v82, v109, v108, s33
	s_waitcnt lgkmcnt(0)
	v_perm_b32 v83, v81, v80, s33
	v_perm_b32 v107, v81, v80, s76
	v_cvt_scalef32_pk_bf16_fp8 v80, v82, 1.0
	v_cvt_scalef32_pk_bf16_fp8 v81, v82, 1.0 op_sel:[1,0,0]
	v_cvt_scalef32_pk_bf16_fp8 v82, v83, 1.0
	v_cvt_scalef32_pk_bf16_fp8 v83, v83, 1.0 op_sel:[1,0,0]
	v_cvt_scalef32_pk_bf16_fp8 v106, v107, 1.0
	v_cvt_scalef32_pk_bf16_fp8 v107, v107, 1.0 op_sel:[1,0,0]
	v_mfma_f32_16x16x32_bf16 v[80:83], v[0:3], v[80:83], v[84:87]
	s_nop 0
	v_mfma_f32_16x16x32_bf16 v[84:87], v[0:3], v[104:107], v[92:95]
	s_nop 2
	ds_read_b64_tr_b16 v[92:93], v181 offset:9280
	ds_read_b64_tr_b16 v[94:95], v181 offset:11584
	s_waitcnt lgkmcnt(1)
	v_perm_b32 v104, v93, v92, s33
	s_waitcnt lgkmcnt(0)
	v_perm_b32 v106, v95, v94, s33
	v_perm_b32 v105, v93, v92, s76
	v_perm_b32 v107, v95, v94, s76
	v_cvt_scalef32_pk_bf16_fp8 v92, v104, 1.0
	v_cvt_scalef32_pk_bf16_fp8 v93, v104, 1.0 op_sel:[1,0,0]
	v_cvt_scalef32_pk_bf16_fp8 v94, v106, 1.0
	v_cvt_scalef32_pk_bf16_fp8 v95, v106, 1.0 op_sel:[1,0,0]
	v_cvt_scalef32_pk_bf16_fp8 v108, v105, 1.0
	v_cvt_scalef32_pk_bf16_fp8 v109, v105, 1.0 op_sel:[1,0,0]
	v_cvt_scalef32_pk_bf16_fp8 v110, v107, 1.0
	v_cvt_scalef32_pk_bf16_fp8 v111, v107, 1.0 op_sel:[1,0,0]
	v_mfma_f32_16x16x32_bf16 v[104:107], v[0:3], v[92:95], v[96:99]
	ds_read_b64_tr_b16 v[92:93], v181 offset:9312
	ds_read_b64_tr_b16 v[94:95], v181 offset:11616
	s_waitcnt vmcnt(15)
	ds_write_b128 v205, v[4:7]
	s_waitcnt vmcnt(14)
	ds_write_b128 v205, v[8:11] offset:1152
	s_waitcnt vmcnt(13)
	ds_write_b128 v205, v[12:15] offset:2304
	s_waitcnt vmcnt(12)
	ds_write_b128 v205, v[68:71] offset:3456
	s_waitcnt lgkmcnt(5)
	v_perm_b32 v96, v93, v92, s33
	v_perm_b32 v97, v93, v92, s76
	s_waitcnt lgkmcnt(4)
	v_perm_b32 v98, v95, v94, s33
	v_perm_b32 v99, v95, v94, s76
	v_cvt_scalef32_pk_bf16_fp8 v92, v96, 1.0
	v_cvt_scalef32_pk_bf16_fp8 v93, v96, 1.0 op_sel:[1,0,0]
	v_cvt_scalef32_pk_bf16_fp8 v94, v98, 1.0
	v_cvt_scalef32_pk_bf16_fp8 v95, v98, 1.0 op_sel:[1,0,0]
	v_cvt_scalef32_pk_bf16_fp8 v96, v97, 1.0
	v_cvt_scalef32_pk_bf16_fp8 v97, v97, 1.0 op_sel:[1,0,0]
	v_cvt_scalef32_pk_bf16_fp8 v98, v99, 1.0
	v_cvt_scalef32_pk_bf16_fp8 v99, v99, 1.0 op_sel:[1,0,0]
	v_mfma_f32_16x16x32_bf16 v[108:111], v[0:3], v[108:111], v[100:103]
	v_mfma_f32_16x16x32_bf16 v[112:115], v[0:3], v[92:95], v[112:115]
	v_mfma_f32_16x16x32_bf16 v[116:119], v[0:3], v[96:99], v[88:91]
	ds_read_u16 v0, v159
	ds_read_u16 v4, v159 offset:16
	ds_read_u16 v8, v159 offset:32
	ds_read_u16 v12, v159 offset:48
	s_waitcnt lgkmcnt(3)
	v_lshl_or_b32 v0, v0, 9, v182
	s_waitcnt lgkmcnt(2)
	v_lshl_or_b32 v4, v4, 9, v182
	s_waitcnt lgkmcnt(1)
	v_lshl_or_b32 v8, v8, 9, v182
	s_waitcnt lgkmcnt(0)
	v_lshl_or_b32 v12, v12, 9, v182
	global_load_dwordx4 v[0:3], v0, s[48:49]
	s_nop 0
	global_load_dwordx4 v[4:7], v4, s[48:49]
	s_nop 0
	global_load_dwordx4 v[8:11], v8, s[48:49]
	s_nop 0
	global_load_dwordx4 v[12:15], v12, s[48:49]
	ds_read_b64_tr_b16 v[68:69], v181 offset:2304
	ds_read_b64_tr_b16 v[70:71], v181
	ds_read_b64_tr_b16 v[96:97], v181 offset:32
	s_waitcnt lgkmcnt(2)
	v_perm_b32 v90, v69, v68, s76
	s_waitcnt lgkmcnt(1)
	v_perm_b32 v88, v71, v70, s33
	v_perm_b32 v89, v71, v70, s76
	v_perm_b32 v71, v69, v68, s33
	v_cvt_scalef32_pk_bf16_fp8 v68, v88, 1.0
	v_cvt_scalef32_pk_bf16_fp8 v69, v88, 1.0 op_sel:[1,0,0]
	v_cvt_scalef32_pk_bf16_fp8 v70, v71, 1.0
	v_cvt_scalef32_pk_bf16_fp8 v71, v71, 1.0 op_sel:[1,0,0]
	v_cvt_scalef32_pk_bf16_fp8 v92, v89, 1.0
	v_cvt_scalef32_pk_bf16_fp8 v93, v89, 1.0 op_sel:[1,0,0]
	v_cvt_scalef32_pk_bf16_fp8 v94, v90, 1.0
	v_cvt_scalef32_pk_bf16_fp8 v95, v90, 1.0 op_sel:[1,0,0]
	v_mfma_f32_16x16x32_bf16 v[88:91], v[16:19], v[68:71], v[72:75]
	ds_read_b64_tr_b16 v[68:69], v181 offset:2336
	s_waitcnt lgkmcnt(1)
	v_perm_b32 v70, v97, v96, s33
	s_waitcnt lgkmcnt(0)
	v_perm_b32 v71, v69, v68, s33
	v_perm_b32 v75, v69, v68, s76
	v_cvt_scalef32_pk_bf16_fp8 v68, v70, 1.0
	v_cvt_scalef32_pk_bf16_fp8 v69, v70, 1.0 op_sel:[1,0,0]
	v_cvt_scalef32_pk_bf16_fp8 v70, v71, 1.0
	v_cvt_scalef32_pk_bf16_fp8 v71, v71, 1.0 op_sel:[1,0,0]
	v_perm_b32 v73, v97, v96, s76
	v_cvt_scalef32_pk_bf16_fp8 v72, v73, 1.0
	v_mfma_f32_16x16x32_bf16 v[96:99], v[16:19], v[68:71], v[80:83]
	ds_read_b64_tr_b16 v[68:69], v181 offset:64
	ds_read_b64_tr_b16 v[70:71], v181 offset:2368
	v_cvt_scalef32_pk_bf16_fp8 v73, v73, 1.0 op_sel:[1,0,0]
	v_cvt_scalef32_pk_bf16_fp8 v74, v75, 1.0
	v_cvt_scalef32_pk_bf16_fp8 v75, v75, 1.0 op_sel:[1,0,0]
	v_mfma_f32_16x16x32_bf16 v[92:95], v[16:19], v[92:95], v[76:79]
	s_nop 0
	v_mfma_f32_16x16x32_bf16 v[100:103], v[16:19], v[72:75], v[84:87]
	s_waitcnt lgkmcnt(1)
	v_perm_b32 v72, v69, v68, s33
	s_waitcnt lgkmcnt(0)
	v_perm_b32 v74, v71, v70, s33
	v_perm_b32 v73, v69, v68, s76
	v_perm_b32 v75, v71, v70, s76
	v_cvt_scalef32_pk_bf16_fp8 v68, v72, 1.0
	v_cvt_scalef32_pk_bf16_fp8 v69, v72, 1.0 op_sel:[1,0,0]
	v_cvt_scalef32_pk_bf16_fp8 v70, v74, 1.0
	v_cvt_scalef32_pk_bf16_fp8 v71, v74, 1.0 op_sel:[1,0,0]
	v_cvt_scalef32_pk_bf16_fp8 v72, v73, 1.0
	v_cvt_scalef32_pk_bf16_fp8 v73, v73, 1.0 op_sel:[1,0,0]
	v_mfma_f32_16x16x32_bf16 v[104:107], v[16:19], v[68:71], v[104:107]
	ds_read_b64_tr_b16 v[68:69], v181 offset:96
	ds_read_b64_tr_b16 v[70:71], v181 offset:2400
	v_cvt_scalef32_pk_bf16_fp8 v74, v75, 1.0
	v_cvt_scalef32_pk_bf16_fp8 v75, v75, 1.0 op_sel:[1,0,0]
	s_waitcnt vmcnt(15)
	ds_write_b128 v205, v[20:23] offset:9216
	s_waitcnt vmcnt(14)
	ds_write_b128 v205, v[24:27] offset:10368
	s_waitcnt vmcnt(13)
	ds_write_b128 v205, v[28:31] offset:11520
	s_waitcnt vmcnt(12)
	ds_write_b128 v205, v[64:67] offset:12672
	v_mfma_f32_16x16x32_bf16 v[108:111], v[16:19], v[72:75], v[108:111]
	s_waitcnt lgkmcnt(5)
	v_perm_b32 v72, v69, v68, s33
	v_perm_b32 v73, v69, v68, s76
	s_waitcnt lgkmcnt(4)
	v_perm_b32 v74, v71, v70, s33
	v_perm_b32 v75, v71, v70, s76
	v_cvt_scalef32_pk_bf16_fp8 v68, v72, 1.0
	v_cvt_scalef32_pk_bf16_fp8 v69, v72, 1.0 op_sel:[1,0,0]
	v_cvt_scalef32_pk_bf16_fp8 v70, v74, 1.0
	v_cvt_scalef32_pk_bf16_fp8 v71, v74, 1.0 op_sel:[1,0,0]
	v_cvt_scalef32_pk_bf16_fp8 v72, v73, 1.0
	v_cvt_scalef32_pk_bf16_fp8 v73, v73, 1.0 op_sel:[1,0,0]
	v_cvt_scalef32_pk_bf16_fp8 v74, v75, 1.0
	v_cvt_scalef32_pk_bf16_fp8 v75, v75, 1.0 op_sel:[1,0,0]
	v_mfma_f32_16x16x32_bf16 v[112:115], v[16:19], v[68:71], v[112:115]
	s_nop 0
	v_mfma_f32_16x16x32_bf16 v[116:119], v[16:19], v[72:75], v[116:119]
	ds_read_u16 v16, v159 offset:64
	ds_read_u16 v17, v159 offset:80
	ds_read_u16 v20, v159 offset:96
	ds_read_u16 v24, v159 offset:112
	s_waitcnt lgkmcnt(3)
	v_lshl_or_b32 v16, v16, 9, v182
	global_load_dwordx4 v[28:31], v16, s[48:49]
	s_waitcnt lgkmcnt(1)
	v_lshl_or_b32 v20, v20, 9, v182
	global_load_dwordx4 v[20:23], v20, s[48:49]
	v_lshl_or_b32 v16, v17, 9, v182
	s_waitcnt lgkmcnt(0)
	v_lshl_or_b32 v24, v24, 9, v182
	global_load_dwordx4 v[16:19], v16, s[48:49]
	s_nop 0
	global_load_dwordx4 v[24:27], v24, s[48:49]
	s_mul_i32 s6, s10, 0x1100
	v_add_u32_e32 v64, s6, v183
	v_lshl_add_u32 v80, v64, 1, v164
	v_mov_b32_e32 v68, 0
	v_mov_b32_e32 v64, 0
	v_mov_b32_e32 v65, 0
	v_mov_b32_e32 v66, 0
	v_mov_b32_e32 v67, 0
	s_and_saveexec_b64 s[6:7], s[38:39]
	s_cbranch_execz .LBB0_547
	global_load_dwordx4 v[64:67], v80, s[44:45]
